# v040 + phase 0: odd waves run the short latency-bound items (transposes, tables, p conversion) first and the expert-weight stream after; even waves keep the order
# baseline (speedup 1.0000x reference)
; #define LAS __attribute__((address_space(3)))
; __global__ void __launch_bounds__(NTHR, 2) mk_fwd(Args args) {
;     extern __shared__ __attribute__((aligned(16))) unsigned char lds_raw[];
;     LAS unsigned char* lds = (LAS unsigned char*)lds_raw;
;     const int G = gridDim.x;
;     const int vcu = (G % 8 == 0) ? ((int)blockIdx.x % 8) * (G / 8) + (int)blockIdx.x / 8 : (int)blockIdx.x;
;     volatile LAS unsigned* MISC = (volatile LAS unsigned*)(lds + LDS_MISC);
;     LAS int* blkoff = (LAS int*)(lds + LDS_TBL);
;     if (threadIdx.x < 4) MISC[threadIdx.x] = 0u;
;     __syncthreads();
_Z6mk_fwd4Args:
	s_mov_b64 s[76:77], s[0:1]
	s_load_dword s68, s[0:1], 0xf0
	s_nop 0
	s_load_dwordx2 s[0:1], s[0:1], 0xd8
	s_nop 0
	s_load_dwordx4 s[56:59], s[76:77], 0xe0
	s_add_u32 s4, s76, 0xf0
	s_addc_u32 s5, s77, 0
	s_waitcnt lgkmcnt(0)
	s_and_b32 s3, s68, 7
	v_writelane_b32 v253, s4, 0
	s_cmp_lg_u32 s3, 0
	s_mov_b32 s86, s2
	s_mov_b32 s8, 0
	s_nop 0
	v_writelane_b32 v255, s8, 61
	v_writelane_b32 v253, s5, 1
	s_cbranch_scc0 .LBB0_117
	v_cmp_gt_u32_e32 vcc, 4, v0
	s_and_saveexec_b64 s[4:5], vcc

; #define LAS __attribute__((address_space(3)))
; __device__ __forceinline__ void phase_p0a(const Ptrs& P, LAS unsigned char* lds, int tid_, int vcu, int G) {
;     ...
;     __syncthreads();
;     { LAS unsigned char* img = lds + (wave < 7 ? wave * 18432 : LDS_ROWTAB);
;       constexpr int NI_E = 96, NI_EL = NE * NI_E;
;       auto mk = [&](int it) { Item8 I;
;         const int l = NL - 1 - it / NI_EL, r = it % NI_EL, e = r / NI_E, q = r % NI_E, mat = q >> 5, qq = q & 31;
;         const size_t eo = ((size_t)l * NE + e) * 1024 * 256;
;         if (mat < 2) { const int k0 = 128 * (qq >> 2), n0 = 64 * (qq & 3); I.src = (mat ? P.ew_up : P.ew_gate) + eo + (size_t)k0 * 256 + n0; I.ldw = 256; I.Kd = 1024; I.perm = 0; I.n0 = n0;
;             I.dst = P.ws + WS_WGU + (size_t)l * WGU_L + (size_t)(e * 512 + 128 * mat) * 1024 + k0; }
;         else { const int k0 = 128 * (qq >> 4), n0 = 64 * (qq & 15); I.src = P.ew_down + eo + (size_t)k0 * 1024 + n0; I.ldw = 1024; I.Kd = 256; I.perm = 1; I.n0 = n0;
;             I.dst = P.ws + WS_WD + (size_t)l * WD_L + WD8_OFF + (size_t)(e * 1024) * 256 + k0; }
;         return I; };
;       f32x4 r[32]; int it = gw; Item8 cur = mk(it < NL * NI_EL ? it : 0);
;       if (it < NL * NI_EL) item8_load(cur, r, lane);
.Lp0a_stream:
	v_ashrrev_i32_e32 v10, 6, v130
	v_lshl_add_u32 v1, s86, 3, v10
	s_mov_b32 s4, 0xc000
	v_cmp_gt_i32_e32 vcc, s4, v1
	s_mov_b32 s4, 0xd5555555
	s_waitcnt lgkmcnt(0)
	v_cndmask_b32_e32 v3, 0, v1, vcc
	v_mul_hi_i32 v2, v3, s4
	v_lshrrev_b32_e32 v4, 31, v2
	v_ashrrev_i32_e32 v2, 11, v2
	s_mov_b32 s4, 0x2aaaaaab
	v_add3_u32 v2, v2, v4, 3
	v_mul_hi_i32 v4, v3, s4
	v_lshrrev_b32_e32 v5, 31, v4
	v_ashrrev_i32_e32 v4, 11, v4
	v_add_u32_e32 v4, v4, v5
	v_mul_i32_i24_e32 v4, 0x3000, v4
	v_sub_u32_e32 v3, v3, v4
	s_movk_i32 s4, 0x2aab
	v_mul_i32_i24_sdwa v4, sext(v3), s4 dst_sel:DWORD dst_unused:UNUSED_PAD src0_sel:WORD_0 src1_sel:DWORD
	v_lshrrev_b32_e32 v5, 31, v4
	v_ashrrev_i32_e32 v4, 20, v4
	v_add_u16_e32 v11, v4, v5
	v_mul_lo_u16_e32 v5, 0x60, v11
	v_sub_u16_e32 v13, v3, v5
	v_mov_b32_e32 v3, 5
	v_bfe_i32 v4, v11, 0, 16
	v_ashrrev_i32_sdwa v12, v3, sext(v13) dst_sel:DWORD dst_unused:UNUSED_PAD src0_sel:DWORD src1_sel:WORD_0
	v_mov_b32_e32 v3, 31
	v_and_b32_sdwa v14, sext(v13), v3 dst_sel:DWORD dst_unused:UNUSED_PAD src0_sel:WORD_0 src1_sel:DWORD
	v_mov_b32_e32 v3, 0
	v_ashrrev_i32_e32 v5, 31, v4
	v_lshlrev_b64 v[4:5], 18, v[4:5]
	v_lshlrev_b64 v[6:7], 25, v[2:3]
	v_lshl_add_u64 v[6:7], v[4:5], 0, v[6:7]
	v_mov_b32_e32 v4, 6
	v_cmp_lt_i32_e64 s[4:5], 1, v12
	v_lshlrev_b32_sdwa v15, v4, sext(v13) dst_sel:DWORD dst_unused:UNUSED_PAD src0_sel:DWORD src1_sel:WORD_0
	v_readlane_b32 s6, v255, 61
	s_nop 3
	s_cmp_eq_u32 s6, 2
	s_cbranch_scc1 .Lp0a_skipbar
	s_barrier
.Lp0a_skipbar:
	s_and_saveexec_b64 s[6:7], s[4:5]
	s_xor_b64 s[4:5], exec, s[6:7]
	s_cbranch_execz .LBB0_16
	v_lshlrev_b32_e32 v4, 3, v14
	v_and_b32_e32 v138, 0x80, v4
	v_and_b32_e32 v149, 0x3c0, v15
	v_lshl_add_u64 v[4:5], v[6:7], 2, s[12:13]
	v_lshlrev_b32_e32 v6, 12, v138
	v_mov_b32_e32 v7, v3
	v_lshl_add_u64 v[4:5], v[4:5], 0, v[6:7]
	v_lshlrev_b32_e32 v6, 2, v149
	v_lshl_add_u64 v[4:5], v[4:5], 0, v[6:7]
	s_mov_b32 s6, 0x4080000
	v_mov_b64_e32 v[6:7], s[0:1]
	v_mov_b32_e32 v139, v3
	v_mad_u64_u32 v[2:3], s[6:7], v2, s6, v[6:7]
	s_mov_b64 s[6:7], 0x24100000
	s_nop 0
	v_lshl_add_u64 v[140:141], v[2:3], 0, s[6:7]
	v_mov_b32_e32 v2, 10
	v_lshlrev_b32_sdwa v142, v2, sext(v11) dst_sel:DWORD dst_unused:UNUSED_PAD src0_sel:DWORD src1_sel:WORD_0

; __device__ __forceinline__ void item8_load(const Item8& I, f32x4 (&r)[32], int lane) {
;     const float* src = I.src + (size_t)(lane >> 4) * I.ldw + 4 * (lane & 15);
; #pragma unroll
;     for (int i = 0; i < 32; ++i) r[i] = __builtin_nontemporal_load((const f32x4*)(src + (size_t)(4 * i) * I.ldw));
; }
; __device__ __forceinline__ void phase_p0a(const Ptrs& P, LAS unsigned char* lds, int tid_, int vcu, int G) {
;     ...
;       f32x4 r[32]; int it = gw; Item8 cur = mk(it < NL * NI_EL ? it : 0);
;       if (it < NL * NI_EL) item8_load(cur, r, lane);
;       for (; it < NL * NI_EL; it += NGW) {
.LBB0_18:
	s_or_b64 exec, exec, s[6:7]
	s_movk_i32 s4, 0x4800
	v_mul_lo_u32 v2, v10, s4
	v_mov_b32_e32 v3, 0x21000
	v_cmp_gt_i32_e64 s[4:5], 7, v10
	v_and_b32_e32 v133, 63, v130
	s_lshl_b32 s33, s68, 3
	v_cndmask_b32_e64 v131, v3, v2, s[4:5]
	v_add_u32_e32 v160, 0, v131
	v_lshlrev_b32_e32 v132, 2, v133
	v_lshlrev_b32_e32 v161, 3, v133
	v_readfirstlane_b32 s4, v10
	v_readlane_b32 s5, v255, 61
	s_nop 3
	s_and_b32 s4, s4, 1
	s_cmp_eq_u32 s4, 1
	s_cbranch_scc0 .Lp0a_j1_done
	s_cmp_eq_u32 s5, 0
	s_cbranch_scc0 .Lp0a_j1_done
	s_mov_b32 s5, 1
	s_nop 0
	v_writelane_b32 v255, s5, 61
	s_mov_b64 s[38:39], exec
	s_branch .LBB0_43
.Lp0a_j1_done:
	s_and_saveexec_b64 s[38:39], vcc
	s_cbranch_execz .LBB0_43
	v_lshrrev_b32_e32 v162, 4, v133
	v_mul_u32_u24_e32 v2, v8, v162
	v_lshlrev_b32_e32 v134, 2, v2
	v_mov_b32_e32 v135, 0
	v_and_b32_e32 v146, 60, v132
	v_lshl_add_u64 v[2:3], v[4:5], 0, v[134:135]
	v_lshlrev_b32_e32 v134, 2, v146
	v_lshl_add_u64 v[10:11], v[2:3], 0, v[134:135]
	v_lshlrev_b32_e32 v134, 4, v8
	v_lshl_add_u64 v[12:13], v[10:11], 0, v[134:135]
	v_lshl_add_u64 v[18:19], v[12:13], 0, v[134:135]
	v_lshl_add_u64 v[20:21], v[18:19], 0, v[134:135]
	v_lshl_add_u64 v[26:27], v[20:21], 0, v[134:135]
	v_lshl_add_u64 v[28:29], v[26:27], 0, v[134:135]
	v_lshl_add_u64 v[34:35], v[28:29], 0, v[134:135]
	v_lshl_add_u64 v[36:37], v[34:35], 0, v[134:135]
	v_lshl_add_u64 v[38:39], v[36:37], 0, v[134:135]
	v_lshl_add_u64 v[40:41], v[38:39], 0, v[134:135]
	v_lshl_add_u64 v[42:43], v[40:41], 0, v[134:135]
	v_lshl_add_u64 v[46:47], v[42:43], 0, v[134:135]
	v_lshl_add_u64 v[50:51], v[46:47], 0, v[134:135]
	v_lshl_add_u64 v[54:55], v[50:51], 0, v[134:135]
	v_lshl_add_u64 v[58:59], v[54:55], 0, v[134:135]
	v_lshl_add_u64 v[62:63], v[58:59], 0, v[134:135]
	v_lshl_add_u64 v[66:67], v[62:63], 0, v[134:135]
	v_lshl_add_u64 v[70:71], v[66:67], 0, v[134:135]
	v_lshl_add_u64 v[74:75], v[70:71], 0, v[134:135]
	v_lshl_add_u64 v[78:79], v[74:75], 0, v[134:135]
	v_lshl_add_u64 v[82:83], v[78:79], 0, v[134:135]
	v_lshl_add_u64 v[86:87], v[82:83], 0, v[134:135]
	v_lshl_add_u64 v[90:91], v[86:87], 0, v[134:135]
	v_lshl_add_u64 v[94:95], v[90:91], 0, v[134:135]
	v_lshl_add_u64 v[98:99], v[94:95], 0, v[134:135]
	v_lshl_add_u64 v[102:103], v[98:99], 0, v[134:135]
	v_lshl_add_u64 v[106:107], v[102:103], 0, v[134:135]
	v_lshl_add_u64 v[110:111], v[106:107], 0, v[134:135]
	v_lshl_add_u64 v[114:115], v[110:111], 0, v[134:135]
	v_lshl_add_u64 v[118:119], v[114:115], 0, v[134:135]
	v_lshl_add_u64 v[122:123], v[118:119], 0, v[134:135]
	v_lshl_add_u64 v[126:127], v[122:123], 0, v[134:135]
	global_load_dwordx4 v[2:5], v[10:11], off nt
	global_load_dwordx4 v[6:9], v[12:13], off nt
	s_nop 0
	global_load_dwordx4 v[10:13], v[18:19], off nt
	global_load_dwordx4 v[14:17], v[20:21], off nt
	s_nop 0
	global_load_dwordx4 v[18:21], v[26:27], off nt
	global_load_dwordx4 v[22:25], v[28:29], off nt
	s_nop 0
	global_load_dwordx4 v[26:29], v[34:35], off nt
	global_load_dwordx4 v[30:33], v[36:37], off nt
	v_ashrrev_i32_e32 v143, 31, v142
	global_load_dwordx4 v[34:37], v[38:39], off nt
	v_lshlrev_b64 v[142:143], v144, v[142:143]
	global_load_dwordx4 v[38:41], v[40:41], off nt
	v_lshl_add_u64 v[140:141], v[140:141], 0, v[142:143]
	global_load_dwordx4 v[42:45], v[42:43], off nt
	v_lshl_add_u64 v[142:143], v[140:141], 0, v[138:139]
	global_load_dwordx4 v[46:49], v[46:47], off nt
	v_and_b32_e32 v138, 48, v130
	global_load_dwordx4 v[50:53], v[50:51], off nt
	v_bfe_u32 v139, v130, 2, 2
	global_load_dwordx4 v[54:57], v[54:55], off nt
	s_movk_i32 s4, 0x90
	global_load_dwordx4 v[58:61], v[58:59], off nt
	v_or_b32_e32 v139, v139, v138
	global_load_dwordx4 v[62:65], v[62:63], off nt
	v_mad_u32_u24 v134, v162, s4, v160
	global_load_dwordx4 v[66:69], v[66:67], off nt
	v_and_b32_e32 v140, 0x78, v161
	global_load_dwordx4 v[70:73], v[70:71], off nt
	v_and_b32_e32 v163, 15, v130
	global_load_dwordx4 v[74:77], v[74:75], off nt
	v_mad_u32_u24 v141, v139, s4, v160
	global_load_dwordx4 v[78:81], v[78:79], off nt
	v_and_b32_e32 v144, 24, v161
	global_load_dwordx4 v[82:85], v[82:83], off nt
	s_add_u32 s40, s0, 0x4000000
	global_load_dwordx4 v[86:89], v[86:87], off nt
	v_mov_b32_e32 v139, v135
	global_load_dwordx4 v[90:93], v[90:91], off nt
	v_or_b32_e32 v164, 16, v163
	global_load_dwordx4 v[94:97], v[94:95], off nt
	v_or_b32_e32 v165, 32, v163
	global_load_dwordx4 v[98:101], v[98:99], off nt
	v_or_b32_e32 v166, 48, v133
	global_load_dwordx4 v[102:105], v[102:103], off nt
	s_addc_u32 s41, s1, 0
	global_load_dwordx4 v[106:109], v[106:107], off nt
	s_mov_b64 s[42:43], 0
	global_load_dwordx4 v[110:113], v[110:111], off nt
	v_add_u32_e32 v167, v134, v140
	global_load_dwordx4 v[114:117], v[114:115], off nt
	s_mov_b32 s48, 0xbfff
	global_load_dwordx4 v[118:121], v[118:119], off nt
	s_nop 0
	global_load_dwordx4 v[122:125], v[122:123], off nt
	s_nop 0
	global_load_dwordx4 v[126:129], v[126:127], off nt
	s_mov_b32 s49, 0xc000
	s_mov_b32 s50, 0xd5555555
	s_mov_b32 s51, 0x2aaaaaab
	s_movk_i32 s52, 0x2aab
	s_mov_b32 s53, 0x4080000
	s_mov_b64 s[44:45], 0x24100000
	v_lshlrev_b32_e32 v140, 2, v146
	s_mov_b32 s54, 0x7fffff00
	v_mov_b32_e32 v168, 5
	v_mov_b32_e32 v169, 31
	v_mov_b32_e32 v170, 6
	v_mov_b32_e32 v171, 10
	v_mov_b32_e32 v172, 9
	v_add_u32_e32 v173, v141, v144
	v_mov_b32_e32 v174, v1
	s_branch .LBB0_21

; __device__ __forceinline__ void phase_p0a(const Ptrs& P, LAS unsigned char* lds, int tid_, int vcu, int G) {
;     ...
;       for (; it < NL * NI_EL; it += NGW) {
;         item8_to_lds(r, img, lane);
;         const bool more = it + NGW < NL * NI_EL; Item8 nxt = mk(more ? it + NGW : it);
;         if (more) item8_load(nxt, r, lane);
;         item8_store(cur, img, lane);
;         cur = nxt;
;       } }
;     constexpr int NI_WIN = 1024, NI_WOUT = 512, NI_ROUT = 64, NI_PLEIN = 128, NI_PLEG = 512, NI_SH = 384, NI_EXP = 0, NI_L = NI_WIN + NI_WOUT + NI_ROUT + NI_PLEIN + NI_PLEG + NI_SH + NI_EXP;
;     for (int it = gw; it < NL * NI_L; it += NGW) {
;         const int l = NL - 1 - it / NI_L; int r = it % NI_L;
;         if (r >= NI_L - NI_EXP - NI_SH) {
;             r -= NI_L - NI_EXP - NI_SH;
;             int eidx, q; const float *sg, *su, *sd;
;             { eidx = 0; q = r; sg = P.sh_gate + (size_t)l * 1024 * 256; su = P.sh_up + (size_t)l * 1024 * 256; sd = P.sh_down + (size_t)l * 256 * 1024; }
;             if (q < 256) { const int up = q >> 7, qq = q & 127, kb = qq >> 3, nb = qq & 7, n0 = 32 * nb, k0 = 64 * kb;
.LBB0_43:
	s_or_b64 exec, exec, s[38:39]
	v_readlane_b32 s4, v255, 61
	s_nop 3
	s_cmp_eq_u32 s4, 2
	s_cbranch_scc1 .Lp0a_fin
	s_movk_i32 s4, 0x2900
	v_cmp_gt_i32_e32 vcc, s4, v1
	s_and_saveexec_b64 s[4:5], vcc
	s_cbranch_execz .LBB0_84
	s_add_u32 s6, s0, 0x2500000
	s_addc_u32 s7, s1, 0
	s_add_u32 s8, s0, 0x2300000
	s_addc_u32 s9, s1, 0
	s_add_u32 s10, s0, 0x1d00000
	s_addc_u32 s11, s1, 0
	s_add_u32 s12, s0, 0x1500000
	s_addc_u32 s13, s1, 0
	s_waitcnt vmcnt(38)
	v_lshrrev_b32_e32 v9, 3, v133
	v_and_b32_e32 v4, 56, v161
	s_add_u32 s38, s0, 0x100000
	v_lshrrev_b32_e32 v5, 5, v133
	v_and_b32_e32 v2, 31, v130
	v_mov_b32_e32 v3, 0
	s_movk_i32 s42, 0x84
	v_mul_u32_u24_e32 v6, 0x84, v4
	v_lshlrev_b32_e32 v7, 2, v9
	s_addc_u32 s39, s1, 0
	v_add3_u32 v7, v160, v6, v7
	v_lshlrev_b32_e32 v6, 10, v9
	s_waitcnt vmcnt(37)
	v_or_b32_e32 v11, 8, v9
	v_or_b32_e32 v13, 16, v9
	s_waitcnt vmcnt(36)
	v_or_b32_e32 v15, 24, v9
	v_lshlrev_b32_e32 v14, 8, v9
	s_add_u32 s40, s0, 0x24000000
	v_mad_u32_u24 v9, v5, s42, v131
	s_waitcnt vmcnt(34)
	v_lshlrev_b32_e32 v22, 2, v2
	v_mov_b32_e32 v23, v3
	v_lshlrev_b32_e32 v8, 10, v11
	v_lshlrev_b32_e32 v10, 10, v13
	v_lshlrev_b32_e32 v12, 10, v15
	v_lshlrev_b32_e32 v16, 8, v11
	v_lshlrev_b32_e32 v18, 8, v13
	v_lshlrev_b32_e32 v20, 8, v15
	s_addc_u32 s41, s1, 0
	v_add3_u32 v9, v9, v22, 0
	v_lshl_add_u64 v[24:25], s[22:23], 0, v[22:23]
	v_or_b32_e32 v11, 0xfffff28e, v5
	v_or_b32_e32 v13, 0xfffff28c, v5
	v_or_b32_e32 v15, 0xfffff28a, v5
	v_or_b32_e32 v17, 0xfffff288, v5
	v_or_b32_e32 v19, 0xfffff286, v5
	v_or_b32_e32 v21, 0xfffff284, v5
	s_waitcnt vmcnt(27)
	v_or_b32_e32 v52, 0xfffff282, v5
	v_or_b32_e32 v53, 0xfffff280, v5
	v_lshl_add_u64 v[26:27], s[20:21], 0, v[22:23]
	s_waitcnt vmcnt(26)
	v_or_b32_e32 v54, 0xfffff38e, v5
	v_or_b32_e32 v55, 0xfffff38c, v5
	v_or_b32_e32 v56, 0xfffff38a, v5
	v_or_b32_e32 v57, 0xfffff388, v5
	s_waitcnt vmcnt(25)
	v_or_b32_e32 v58, 0xfffff386, v5
	v_or_b32_e32 v59, 0xfffff384, v5
	v_or_b32_e32 v60, 0xfffff382, v5
	v_or_b32_e32 v61, 0xfffff380, v5
	v_lshl_add_u64 v[28:29], s[36:37], 0, v[22:23]
	s_waitcnt vmcnt(24)
	v_or_b32_e32 v62, 0xffffa00e, v5
	v_or_b32_e32 v63, 0xffffa00c, v5
	v_or_b32_e32 v64, 0xffffa00a, v5
	v_or_b32_e32 v65, 0xffffa008, v5
	s_waitcnt vmcnt(23)
	v_or_b32_e32 v66, 0xffffa006, v5
	v_or_b32_e32 v67, 0xffffa004, v5
	v_or_b32_e32 v68, 0xffffa002, v5
	v_or_b32_e32 v69, 0xffffa000, v5
	v_lshl_add_u64 v[30:31], s[34:35], 0, v[22:23]
	s_waitcnt vmcnt(22)
	v_or_b32_e32 v70, 0xfffff80e, v5
	v_or_b32_e32 v71, 0xfffff80c, v5
	v_or_b32_e32 v72, 0xfffff80a, v5
	v_or_b32_e32 v73, 0xfffff808, v5
	s_waitcnt vmcnt(21)
	v_or_b32_e32 v74, 0xfffff806, v5
	v_or_b32_e32 v75, 0xfffff804, v5
	v_or_b32_e32 v76, 0xfffff802, v5
	v_or_b32_e32 v77, 0xfffff800, v5
	v_lshl_add_u64 v[32:33], s[18:19], 0, v[22:23]
	s_waitcnt vmcnt(20)
	v_or_b32_e32 v78, 0xffffec8e, v5
	v_or_b32_e32 v79, 0xffffec8c, v5
	v_or_b32_e32 v80, 0xffffec8a, v5
	v_or_b32_e32 v81, 0xffffec88, v5
	s_waitcnt vmcnt(19)
	v_or_b32_e32 v82, 0xffffec86, v5
	v_or_b32_e32 v83, 0xffffec84, v5
	v_or_b32_e32 v84, 0xffffec82, v5
	v_or_b32_e32 v85, 0xffffec80, v5
	s_waitcnt vmcnt(18)
	v_or_b32_e32 v86, 14, v5
	v_or_b32_e32 v87, 12, v5
	v_or_b32_e32 v88, 10, v5
	v_or_b32_e32 v89, 8, v5
	s_waitcnt vmcnt(17)
	v_or_b32_e32 v90, 6, v5
	v_or_b32_e32 v91, 4, v5
	v_or_b32_e32 v92, 2, v5
	s_mov_b64 s[18:19], 0
	s_mov_b32 s48, 0x9c18f9c1
	s_mov_b32 s49, 0x63e7063f
	s_movk_i32 s50, 0x8c0
	s_movk_i32 s51, 0x3ff
	s_movk_i32 s52, 0x5ff
	s_movk_i32 s53, 0x63f
	s_movk_i32 s54, 0x6bf
	s_mov_b32 s55, 0x180000
	s_mov_b32 s60, 0x910000
	v_lshlrev_b32_e32 v34, 2, v2
	s_movk_i32 s61, 0x2440
	s_movk_i32 s62, 0x9bf
	s_mov_b32 s63, 0x4080000
	s_movk_i32 s64, 0x100
	s_movk_i32 s65, 0x80
	s_mov_b64 s[20:21], 0x1d80000
	s_movk_i32 s66, 0x28ff
	v_mov_b32_e32 v93, 3
	s_branch .LBB0_47

; __device__ __forceinline__ void xcd_barrier(const XcdBarrier& b) {
;     asm volatile("s_waitcnt vmcnt(0)" ::: "memory");
;     __syncthreads();
;     if (threadIdx.x == 0) {
;         unsigned* bar = b.bar;
;         __builtin_amdgcn_s_waitcnt(0);
;         unsigned nloc = b.st[0], nx = b.st[1];
;         if (nloc == 0u) { xcd_barrier_complete(bar, b.x, nloc, nx); b.st[0] = nloc; b.st[1] = nx; }
.LBB0_105:
	s_or_b64 exec, exec, s[4:5]
	v_readlane_b32 s4, v255, 61
	s_nop 3
	s_cmp_eq_u32 s4, 1
	s_cbranch_scc0 .Lp0a_fin
	s_mov_b32 s4, 2
	s_nop 0
	v_writelane_b32 v255, s4, 61
	s_load_dwordx2 s[0:1], s[76:77], 0xd8
	s_load_dwordx16 s[8:23], s[76:77], 0x80
	s_waitcnt lgkmcnt(0)
	s_branch .Lp0a_stream
.Lp0a_fin:
	s_cmp_lt_i32 s57, 2
	s_cbranch_scc1 .LBB0_160
	s_waitcnt vmcnt(0)
	s_barrier
	s_mov_b64 s[0:1], exec
	v_readlane_b32 s4, v253, 2
	v_readlane_b32 s5, v253, 3
	s_and_b64 s[4:5], s[0:1], s[4:5]
	s_mov_b64 exec, s[4:5]
	s_cbranch_execz .LBB0_159
	s_add_i32 s4, 0, 0x20800
	v_mov_b32_e32 v1, s4
	s_waitcnt vmcnt(0) expcnt(0) lgkmcnt(0)
	ds_read_b32 v3, v1
	s_add_i32 s4, 0, 0x20804
	v_mov_b32_e32 v1, s4
	ds_read_b32 v1, v1
	s_waitcnt lgkmcnt(1)
	v_cmp_ne_u32_e32 vcc, 0, v3
	s_cbranch_vccnz .LBB0_123
	v_readlane_b32 s4, v253, 0
	v_readlane_b32 s5, v253, 1
	s_load_dwordx2 s[8:9], s[4:5], 0x4
	s_add_u32 s4, s58, 0x1000
	s_addc_u32 s5, s59, 0
	s_add_u32 s6, s58, 0x1100
	s_addc_u32 s7, s59, 0
	s_waitcnt lgkmcnt(0)
	s_mul_i32 s18, s8, s68
	s_add_u32 s8, s58, 0x1200
	s_mul_i32 s18, s18, s9
	s_addc_u32 s9, s59, 0
	s_add_u32 s10, s58, 0x1300
	s_addc_u32 s11, s59, 0
	s_mov_b32 s19, 1
	v_mov_b32_e32 v17, 0
	s_branch .LBB0_110
